# K-loop back edge (docs 7.11): pointer / counter / exit-test SALU moved ahead of the loop-back barrier, only the branch follows it (6 loops)
# baseline (speedup 1.0000x reference)
; #define PG8_STAGE(bufoff, gbase, voff) do { _Pragma("unroll") for (int _i = 0; _i < 2; ++_i) \
;         __builtin_amdgcn_global_load_lds((const unsigned*)((const char*)(gbase) + (voff)[_i]), (PG8_LAS unsigned*)(lds + (bufoff) + ldsw + _i * 8192), 16, 0, 0); } while (0)
; #define PG8_LDA(dst, b, h) do { _Pragma("unroll") for (int m = 0; m < 4; ++m) { const bf16x8 f0_ = *(const PG8_LAS bf16x8*)(lds + PG8_SA(b, h) + aoff + m * 2048), f1_ = *(const PG8_LAS bf16x8*)(lds + PG8_SA(b, h) + aoff + m * 2048 + 1024); dst[m].set(f0_, f1_); } } while (0)
; #define PG8_WAIT_V(n) asm volatile("s_waitcnt vmcnt(" #n ")" ::: "memory")
; #define PG8_WAIT_L(n) asm volatile("s_waitcnt lgkmcnt(" #n ")" ::: "memory")
; #define PG8_BAR __builtin_amdgcn_s_barrier()
; #define PG8_SCHED __builtin_amdgcn_sched_barrier(0)
; template <class Epi, class Sched, bool ALIGN_EPI = false, bool SP2 = false>
; __device__ __forceinline__ void gemm_phase(PG8_LAS unsigned char* lds, const Gemm g, const Sched& S, const Epi& E) {
;     ...
;         for (int t = 0; t < nt; t += 2) {
;             if constexpr (Epi::MIDK) { if (t == (nt >> 1)) E.mid(acc, cur, wr, wc, fr, fq); }
;             const bool last = (t == nt - 2);
;             const char* a1 = cA + (size_t)(t + 1) * kstep;
;             const char* a2 = last ? nA : cA + (size_t)(t + 2) * kstep; const char* b2 = last ? nB : cB + (size_t)(t + 2) * kstep;
;     ...
;             PG8_LDA(At, 1, 1); PG8_STAGE(PG8_SB(1, 0), b3, voffB); PG8_STAGE(PG8_SB(1, 1), b3 + hstepB, voffB); PG8_STAGE(PG8_SA(1, 0), a3, voffA);
;             PG8_WAIT_V(8); PG8_WAIT_L(0); PG8_BAR; PG8_MMA(1, 0, At, B0); PG8_MMA(1, 1, At, B1); PG8_BAR; PG8_SCHED;
.Lkr0_b:
	s_waitcnt vmcnt(6)
	s_waitcnt lgkmcnt(0)
	s_barrier
	s_setprio 1
	s_waitcnt lgkmcnt(0)
	v_mfma_scale_f32_16x16x128_f8f6f4 v[94:97], v[2:9], v[212:219], v[94:97], v206, v207 op_sel_hi:[0,0,0]
	v_mfma_scale_f32_16x16x128_f8f6f4 v[90:93], v[10:17], v[212:219], v[90:93], v206, v207 op_sel_hi:[0,0,0]
	v_mfma_scale_f32_16x16x128_f8f6f4 v[78:81], v[2:9], v[220:227], v[78:81], v206, v207 op_sel_hi:[0,0,0]
	v_mfma_scale_f32_16x16x128_f8f6f4 v[74:77], v[10:17], v[220:227], v[74:77], v206, v207 op_sel_hi:[0,0,0]
	v_mfma_scale_f32_16x16x128_f8f6f4 v[62:65], v[2:9], v[228:235], v[62:65], v206, v207 op_sel_hi:[0,0,0]
	v_mfma_scale_f32_16x16x128_f8f6f4 v[58:61], v[10:17], v[228:235], v[58:61], v206, v207 op_sel_hi:[0,0,0]
	v_mfma_scale_f32_16x16x128_f8f6f4 v[46:49], v[2:9], v[236:243], v[46:49], v206, v207 op_sel_hi:[0,0,0]
	v_mfma_scale_f32_16x16x128_f8f6f4 v[42:45], v[10:17], v[236:243], v[42:45], v206, v207 op_sel_hi:[0,0,0]
	v_mfma_scale_f32_16x16x128_f8f6f4 v[86:89], v[18:25], v[212:219], v[86:89], v206, v207 op_sel_hi:[0,0,0]
	v_mfma_scale_f32_16x16x128_f8f6f4 v[82:85], v[26:33], v[212:219], v[82:85], v206, v207 op_sel_hi:[0,0,0]
	v_mfma_scale_f32_16x16x128_f8f6f4 v[70:73], v[18:25], v[220:227], v[70:73], v206, v207 op_sel_hi:[0,0,0]
	v_mfma_scale_f32_16x16x128_f8f6f4 v[66:69], v[26:33], v[220:227], v[66:69], v206, v207 op_sel_hi:[0,0,0]
	v_mfma_scale_f32_16x16x128_f8f6f4 v[54:57], v[18:25], v[228:235], v[54:57], v206, v207 op_sel_hi:[0,0,0]
	v_mfma_scale_f32_16x16x128_f8f6f4 v[50:53], v[26:33], v[228:235], v[50:53], v206, v207 op_sel_hi:[0,0,0]
	v_mfma_scale_f32_16x16x128_f8f6f4 v[38:41], v[18:25], v[236:243], v[38:41], v206, v207 op_sel_hi:[0,0,0]
	v_mfma_scale_f32_16x16x128_f8f6f4 v[34:37], v[26:33], v[236:243], v[34:37], v206, v207 op_sel_hi:[0,0,0]
	s_setprio 0
	s_add_u32 s2, s2, 0x100
	s_addc_u32 s3, s3, 0
	s_add_u32 s20, s20, 0x100
	s_addc_u32 s52, s52, 0
	s_cmp_ge_i32 s53, s69
	s_cselect_b32 s99, 0, 1
	s_mov_b32 s48, s53
	s_barrier
	s_cbranch_scc0 .LBB0_204

; #define PG8_STAGE(bufoff, gbase, voff) do { _Pragma("unroll") for (int _i = 0; _i < 2; ++_i) \
;         __builtin_amdgcn_global_load_lds((const unsigned*)((const char*)(gbase) + (voff)[_i]), (PG8_LAS unsigned*)(lds + (bufoff) + ldsw + _i * 8192), 16, 0, 0); } while (0)
; #define PG8_LDA(dst, b, h) do { _Pragma("unroll") for (int m = 0; m < 4; ++m) { const bf16x8 f0_ = *(const PG8_LAS bf16x8*)(lds + PG8_SA(b, h) + aoff + m * 2048), f1_ = *(const PG8_LAS bf16x8*)(lds + PG8_SA(b, h) + aoff + m * 2048 + 1024); dst[m].set(f0_, f1_); } } while (0)
; #define PG8_WAIT_V(n) asm volatile("s_waitcnt vmcnt(" #n ")" ::: "memory")
; #define PG8_WAIT_L(n) asm volatile("s_waitcnt lgkmcnt(" #n ")" ::: "memory")
; #define PG8_BAR __builtin_amdgcn_s_barrier()
; #define PG8_SCHED __builtin_amdgcn_sched_barrier(0)
; template <class Epi, class Sched, bool ALIGN_EPI = false, bool SP2 = false>
; __device__ __forceinline__ void gemm_phase(PG8_LAS unsigned char* lds, const Gemm g, const Sched& S, const Epi& E) {
;     ...
;         for (int t = 0; t < nt; t += 2) {
;             if constexpr (Epi::MIDK) { if (t == (nt >> 1)) E.mid(acc, cur, wr, wc, fr, fq); }
;             const bool last = (t == nt - 2);
;             const char* a1 = cA + (size_t)(t + 1) * kstep;
;             const char* a2 = last ? nA : cA + (size_t)(t + 2) * kstep; const char* b2 = last ? nB : cB + (size_t)(t + 2) * kstep;
;     ...
;             PG8_LDA(At, 1, 1); PG8_STAGE(PG8_SB(1, 0), b3, voffB); PG8_STAGE(PG8_SB(1, 1), b3 + hstepB, voffB); PG8_STAGE(PG8_SA(1, 0), a3, voffA);
;             PG8_WAIT_V(8); PG8_WAIT_L(0); PG8_BAR; PG8_MMA(1, 0, At, B0); PG8_MMA(1, 1, At, B1); PG8_BAR; PG8_SCHED;
.Lkr2_b:
	s_waitcnt vmcnt(6)
	s_waitcnt lgkmcnt(0)
	s_barrier
	s_setprio 1
	s_waitcnt lgkmcnt(0)
	v_mfma_f32_16x16x32_bf16 v[82:85], v[130:133], v[162:165], v[82:85]
	v_mfma_f32_16x16x32_bf16 v[86:89], v[138:141], v[162:165], v[86:89]
	v_mfma_f32_16x16x32_bf16 v[46:49], v[130:133], v[198:201], v[46:49]
	v_mfma_f32_16x16x32_bf16 v[42:45], v[138:141], v[198:201], v[42:45]
	v_mfma_f32_16x16x32_bf16 v[30:33], v[130:133], v[206:209], v[30:33]
	v_mfma_f32_16x16x32_bf16 v[26:29], v[138:141], v[206:209], v[26:29]
	v_mfma_f32_16x16x32_bf16 v[14:17], v[130:133], v[216:219], v[14:17]
	v_mfma_f32_16x16x32_bf16 v[6:9], v[138:141], v[216:219], v[6:9]
	v_mfma_f32_16x16x32_bf16 v[82:85], v[134:137], v[186:189], v[82:85]
	v_mfma_f32_16x16x32_bf16 v[86:89], v[142:145], v[186:189], v[86:89]
	v_mfma_f32_16x16x32_bf16 v[46:49], v[134:137], v[202:205], v[46:49]
	v_mfma_f32_16x16x32_bf16 v[42:45], v[142:145], v[202:205], v[42:45]
	v_mfma_f32_16x16x32_bf16 v[30:33], v[134:137], v[212:215], v[30:33]
	v_mfma_f32_16x16x32_bf16 v[26:29], v[142:145], v[212:215], v[26:29]
	v_mfma_f32_16x16x32_bf16 v[14:17], v[134:137], v[220:223], v[14:17]
	v_mfma_f32_16x16x32_bf16 v[6:9], v[142:145], v[220:223], v[6:9]
	v_mfma_f32_16x16x32_bf16 v[66:69], v[146:149], v[162:165], v[66:69]
	v_mfma_f32_16x16x32_bf16 v[70:73], v[154:157], v[162:165], v[70:73]
	v_mfma_f32_16x16x32_bf16 v[38:41], v[146:149], v[198:201], v[38:41]
	v_mfma_f32_16x16x32_bf16 v[34:37], v[154:157], v[198:201], v[34:37]
	v_mfma_f32_16x16x32_bf16 v[22:25], v[146:149], v[206:209], v[22:25]
	v_mfma_f32_16x16x32_bf16 v[18:21], v[154:157], v[206:209], v[18:21]
	v_mfma_f32_16x16x32_bf16 v[10:13], v[146:149], v[216:219], v[10:13]
	v_mfma_f32_16x16x32_bf16 v[2:5], v[154:157], v[216:219], v[2:5]
	v_mfma_f32_16x16x32_bf16 v[66:69], v[150:153], v[186:189], v[66:69]
	v_mfma_f32_16x16x32_bf16 v[70:73], v[158:161], v[186:189], v[70:73]
	v_mfma_f32_16x16x32_bf16 v[38:41], v[150:153], v[202:205], v[38:41]
	v_mfma_f32_16x16x32_bf16 v[34:37], v[158:161], v[202:205], v[34:37]
	v_mfma_f32_16x16x32_bf16 v[22:25], v[150:153], v[212:215], v[22:25]
	v_mfma_f32_16x16x32_bf16 v[18:21], v[158:161], v[212:215], v[18:21]
	v_mfma_f32_16x16x32_bf16 v[10:13], v[150:153], v[220:223], v[10:13]
	v_mfma_f32_16x16x32_bf16 v[2:5], v[158:161], v[220:223], v[2:5]
	s_setprio 0
	s_add_u32 s56, s56, 0x100
	s_addc_u32 s57, s57, 0
	s_add_u32 s93, s93, 0x100
	s_addc_u32 s94, s94, 0
	s_cmp_ge_i32 s95, s76
	s_cselect_b32 s99, 0, 1
	s_mov_b32 s58, s95
	s_barrier
	s_cbranch_scc0 .LBB0_1070
	v_readlane_b32 s94, v254, 5
	v_readlane_b32 s95, v254, 6

; #define PG8_STAGE(bufoff, gbase, voff) do { _Pragma("unroll") for (int _i = 0; _i < 2; ++_i) \
;         __builtin_amdgcn_global_load_lds((const unsigned*)((const char*)(gbase) + (voff)[_i]), (PG8_LAS unsigned*)(lds + (bufoff) + ldsw + _i * 8192), 16, 0, 0); } while (0)
; #define PG8_LDA(dst, b, h) do { _Pragma("unroll") for (int m = 0; m < 4; ++m) { const bf16x8 f0_ = *(const PG8_LAS bf16x8*)(lds + PG8_SA(b, h) + aoff + m * 2048), f1_ = *(const PG8_LAS bf16x8*)(lds + PG8_SA(b, h) + aoff + m * 2048 + 1024); dst[m].set(f0_, f1_); } } while (0)
; #define PG8_WAIT_V(n) asm volatile("s_waitcnt vmcnt(" #n ")" ::: "memory")
; #define PG8_WAIT_L(n) asm volatile("s_waitcnt lgkmcnt(" #n ")" ::: "memory")
; #define PG8_BAR __builtin_amdgcn_s_barrier()
; #define PG8_SCHED __builtin_amdgcn_sched_barrier(0)
; template <class Epi, class Sched, bool ALIGN_EPI = false, bool SP2 = false>
; __device__ __forceinline__ void gemm_phase(PG8_LAS unsigned char* lds, const Gemm g, const Sched& S, const Epi& E) {
;     ...
;         for (int t = 0; t < nt; t += 2) {
;             if constexpr (Epi::MIDK) { if (t == (nt >> 1)) E.mid(acc, cur, wr, wc, fr, fq); }
;             const bool last = (t == nt - 2);
;             const char* a1 = cA + (size_t)(t + 1) * kstep;
;             const char* a2 = last ? nA : cA + (size_t)(t + 2) * kstep; const char* b2 = last ? nB : cB + (size_t)(t + 2) * kstep;
;     ...
;             PG8_LDA(At, 1, 1); PG8_STAGE(PG8_SB(1, 0), b3, voffB); PG8_STAGE(PG8_SB(1, 1), b3 + hstepB, voffB); PG8_STAGE(PG8_SA(1, 0), a3, voffA);
;             PG8_WAIT_V(8); PG8_WAIT_L(0); PG8_BAR; PG8_MMA(1, 0, At, B0); PG8_MMA(1, 1, At, B1); PG8_BAR; PG8_SCHED;
.Lkr3_b:
	s_waitcnt vmcnt(6)
	s_waitcnt lgkmcnt(0)
	s_barrier
	s_setprio 1
	s_waitcnt lgkmcnt(0)
	v_mfma_f32_16x16x32_bf16 v[62:65], v[156:159], v[188:191], v[62:65]
	v_mfma_f32_16x16x32_bf16 v[58:61], v[164:167], v[188:191], v[58:61]
	v_mfma_f32_16x16x32_bf16 v[46:49], v[156:159], v[196:199], v[46:49]
	v_mfma_f32_16x16x32_bf16 v[42:45], v[164:167], v[196:199], v[42:45]
	v_mfma_f32_16x16x32_bf16 v[30:33], v[156:159], v[204:207], v[30:33]
	v_mfma_f32_16x16x32_bf16 v[26:29], v[164:167], v[204:207], v[26:29]
	v_mfma_f32_16x16x32_bf16 v[14:17], v[156:159], v[216:219], v[14:17]
	v_mfma_f32_16x16x32_bf16 v[6:9], v[164:167], v[216:219], v[6:9]
	v_mfma_f32_16x16x32_bf16 v[62:65], v[160:163], v[192:195], v[62:65]
	v_mfma_f32_16x16x32_bf16 v[58:61], v[168:171], v[192:195], v[58:61]
	v_mfma_f32_16x16x32_bf16 v[46:49], v[160:163], v[200:203], v[46:49]
	v_mfma_f32_16x16x32_bf16 v[42:45], v[168:171], v[200:203], v[42:45]
	v_mfma_f32_16x16x32_bf16 v[30:33], v[160:163], v[212:215], v[30:33]
	v_mfma_f32_16x16x32_bf16 v[26:29], v[168:171], v[212:215], v[26:29]
	v_mfma_f32_16x16x32_bf16 v[14:17], v[160:163], v[220:223], v[14:17]
	v_mfma_f32_16x16x32_bf16 v[6:9], v[168:171], v[220:223], v[6:9]
	v_mfma_f32_16x16x32_bf16 v[54:57], v[172:175], v[188:191], v[54:57]
	v_mfma_f32_16x16x32_bf16 v[50:53], v[180:183], v[188:191], v[50:53]
	v_mfma_f32_16x16x32_bf16 v[38:41], v[172:175], v[196:199], v[38:41]
	v_mfma_f32_16x16x32_bf16 v[34:37], v[180:183], v[196:199], v[34:37]
	v_mfma_f32_16x16x32_bf16 v[22:25], v[172:175], v[204:207], v[22:25]
	v_mfma_f32_16x16x32_bf16 v[18:21], v[180:183], v[204:207], v[18:21]
	v_mfma_f32_16x16x32_bf16 v[10:13], v[172:175], v[216:219], v[10:13]
	v_mfma_f32_16x16x32_bf16 v[2:5], v[180:183], v[216:219], v[2:5]
	v_mfma_f32_16x16x32_bf16 v[54:57], v[176:179], v[192:195], v[54:57]
	v_mfma_f32_16x16x32_bf16 v[50:53], v[184:187], v[192:195], v[50:53]
	v_mfma_f32_16x16x32_bf16 v[38:41], v[176:179], v[200:203], v[38:41]
	v_mfma_f32_16x16x32_bf16 v[34:37], v[184:187], v[200:203], v[34:37]
	v_mfma_f32_16x16x32_bf16 v[22:25], v[176:179], v[212:215], v[22:25]
	v_mfma_f32_16x16x32_bf16 v[18:21], v[184:187], v[212:215], v[18:21]
	v_mfma_f32_16x16x32_bf16 v[10:13], v[176:179], v[220:223], v[10:13]
	v_mfma_f32_16x16x32_bf16 v[2:5], v[184:187], v[220:223], v[2:5]
	s_setprio 0
	s_add_u32 s30, s30, 0x100
	s_addc_u32 s31, s31, 0
	s_add_u32 s58, s58, 0x100
	s_addc_u32 s59, s59, 0
	s_cmp_ge_i32 s61, s47
	s_cselect_b32 s99, 0, 1
	s_mov_b32 s34, s61
	s_barrier
	s_cbranch_scc0 .LBB0_1171

; #define PG8_STAGE(bufoff, gbase, voff) do { _Pragma("unroll") for (int _i = 0; _i < 2; ++_i) \
;         __builtin_amdgcn_global_load_lds((const unsigned*)((const char*)(gbase) + (voff)[_i]), (PG8_LAS unsigned*)(lds + (bufoff) + ldsw + _i * 8192), 16, 0, 0); } while (0)
; #define PG8_LDA(dst, b, h) do { _Pragma("unroll") for (int m = 0; m < 4; ++m) { const bf16x8 f0_ = *(const PG8_LAS bf16x8*)(lds + PG8_SA(b, h) + aoff + m * 2048), f1_ = *(const PG8_LAS bf16x8*)(lds + PG8_SA(b, h) + aoff + m * 2048 + 1024); dst[m].set(f0_, f1_); } } while (0)
; #define PG8_WAIT_V(n) asm volatile("s_waitcnt vmcnt(" #n ")" ::: "memory")
; #define PG8_WAIT_L(n) asm volatile("s_waitcnt lgkmcnt(" #n ")" ::: "memory")
; #define PG8_BAR __builtin_amdgcn_s_barrier()
; #define PG8_SCHED __builtin_amdgcn_sched_barrier(0)
; template <class Epi, class Sched, bool ALIGN_EPI = false, bool SP2 = false>
; __device__ __forceinline__ void gemm_phase(PG8_LAS unsigned char* lds, const Gemm g, const Sched& S, const Epi& E) {
;     ...
;         for (int t = 0; t < nt; t += 2) {
;             if constexpr (Epi::MIDK) { if (t == (nt >> 1)) E.mid(acc, cur, wr, wc, fr, fq); }
;             const bool last = (t == nt - 2);
;             const char* a1 = cA + (size_t)(t + 1) * kstep;
;             const char* a2 = last ? nA : cA + (size_t)(t + 2) * kstep; const char* b2 = last ? nB : cB + (size_t)(t + 2) * kstep;
;     ...
;             PG8_LDA(At, 1, 1); PG8_STAGE(PG8_SB(1, 0), b3, voffB); PG8_STAGE(PG8_SB(1, 1), b3 + hstepB, voffB); PG8_STAGE(PG8_SA(1, 0), a3, voffA);
;             PG8_WAIT_V(8); PG8_WAIT_L(0); PG8_BAR; PG8_MMA(1, 0, At, B0); PG8_MMA(1, 1, At, B1); PG8_BAR; PG8_SCHED;
.Lkr4_b:
	s_waitcnt vmcnt(6)
	s_waitcnt lgkmcnt(0)
	s_barrier
	s_setprio 1
	s_waitcnt lgkmcnt(0)
	v_mfma_f32_16x16x32_bf16 v[62:65], v[156:159], v[188:191], v[62:65]
	v_mfma_f32_16x16x32_bf16 v[58:61], v[164:167], v[188:191], v[58:61]
	v_mfma_f32_16x16x32_bf16 v[46:49], v[156:159], v[196:199], v[46:49]
	v_mfma_f32_16x16x32_bf16 v[42:45], v[164:167], v[196:199], v[42:45]
	v_mfma_f32_16x16x32_bf16 v[30:33], v[156:159], v[204:207], v[30:33]
	v_mfma_f32_16x16x32_bf16 v[26:29], v[164:167], v[204:207], v[26:29]
	v_mfma_f32_16x16x32_bf16 v[14:17], v[156:159], v[216:219], v[14:17]
	v_mfma_f32_16x16x32_bf16 v[6:9], v[164:167], v[216:219], v[6:9]
	v_mfma_f32_16x16x32_bf16 v[62:65], v[160:163], v[192:195], v[62:65]
	v_mfma_f32_16x16x32_bf16 v[58:61], v[168:171], v[192:195], v[58:61]
	v_mfma_f32_16x16x32_bf16 v[46:49], v[160:163], v[200:203], v[46:49]
	v_mfma_f32_16x16x32_bf16 v[42:45], v[168:171], v[200:203], v[42:45]
	v_mfma_f32_16x16x32_bf16 v[30:33], v[160:163], v[212:215], v[30:33]
	v_mfma_f32_16x16x32_bf16 v[26:29], v[168:171], v[212:215], v[26:29]
	v_mfma_f32_16x16x32_bf16 v[14:17], v[160:163], v[220:223], v[14:17]
	v_mfma_f32_16x16x32_bf16 v[6:9], v[168:171], v[220:223], v[6:9]
	v_mfma_f32_16x16x32_bf16 v[54:57], v[172:175], v[188:191], v[54:57]
	v_mfma_f32_16x16x32_bf16 v[50:53], v[180:183], v[188:191], v[50:53]
	v_mfma_f32_16x16x32_bf16 v[38:41], v[172:175], v[196:199], v[38:41]
	v_mfma_f32_16x16x32_bf16 v[34:37], v[180:183], v[196:199], v[34:37]
	v_mfma_f32_16x16x32_bf16 v[22:25], v[172:175], v[204:207], v[22:25]
	v_mfma_f32_16x16x32_bf16 v[18:21], v[180:183], v[204:207], v[18:21]
	v_mfma_f32_16x16x32_bf16 v[10:13], v[172:175], v[216:219], v[10:13]
	v_mfma_f32_16x16x32_bf16 v[2:5], v[180:183], v[216:219], v[2:5]
	v_mfma_f32_16x16x32_bf16 v[54:57], v[176:179], v[192:195], v[54:57]
	v_mfma_f32_16x16x32_bf16 v[50:53], v[184:187], v[192:195], v[50:53]
	v_mfma_f32_16x16x32_bf16 v[38:41], v[176:179], v[200:203], v[38:41]
	v_mfma_f32_16x16x32_bf16 v[34:37], v[184:187], v[200:203], v[34:37]
	v_mfma_f32_16x16x32_bf16 v[22:25], v[176:179], v[212:215], v[22:25]
	v_mfma_f32_16x16x32_bf16 v[18:21], v[184:187], v[212:215], v[18:21]
	v_mfma_f32_16x16x32_bf16 v[10:13], v[176:179], v[220:223], v[10:13]
	v_mfma_f32_16x16x32_bf16 v[2:5], v[184:187], v[220:223], v[2:5]
	s_setprio 0
	s_add_u32 s30, s30, 0x100
	s_addc_u32 s31, s31, 0
	s_add_u32 s58, s58, 0x100
	s_addc_u32 s59, s59, 0
	s_cmp_ge_i32 s61, s48
	s_cselect_b32 s99, 0, 1
	s_mov_b32 s34, s61
	s_barrier
	s_cbranch_scc0 .LBB0_1592

; #define PG8_STAGE(bufoff, gbase, voff) do { _Pragma("unroll") for (int _i = 0; _i < 2; ++_i) \
;         __builtin_amdgcn_global_load_lds((const unsigned*)((const char*)(gbase) + (voff)[_i]), (PG8_LAS unsigned*)(lds + (bufoff) + ldsw + _i * 8192), 16, 0, 0); } while (0)
; #define PG8_LDA(dst, b, h) do { _Pragma("unroll") for (int m = 0; m < 4; ++m) { const bf16x8 f0_ = *(const PG8_LAS bf16x8*)(lds + PG8_SA(b, h) + aoff + m * 2048), f1_ = *(const PG8_LAS bf16x8*)(lds + PG8_SA(b, h) + aoff + m * 2048 + 1024); dst[m].set(f0_, f1_); } } while (0)
; #define PG8_WAIT_V(n) asm volatile("s_waitcnt vmcnt(" #n ")" ::: "memory")
; #define PG8_WAIT_L(n) asm volatile("s_waitcnt lgkmcnt(" #n ")" ::: "memory")
; #define PG8_BAR __builtin_amdgcn_s_barrier()
; #define PG8_SCHED __builtin_amdgcn_sched_barrier(0)
; template <class Epi, class Sched, bool ALIGN_EPI = false, bool SP2 = false>
; __device__ __forceinline__ void gemm_phase(PG8_LAS unsigned char* lds, const Gemm g, const Sched& S, const Epi& E) {
;     ...
;         for (int t = 0; t < nt; t += 2) {
;             if constexpr (Epi::MIDK) { if (t == (nt >> 1)) E.mid(acc, cur, wr, wc, fr, fq); }
;             const bool last = (t == nt - 2);
;             const char* a1 = cA + (size_t)(t + 1) * kstep;
;             const char* a2 = last ? nA : cA + (size_t)(t + 2) * kstep; const char* b2 = last ? nB : cB + (size_t)(t + 2) * kstep;
;     ...
;             PG8_LDA(At, 1, 1); PG8_STAGE(PG8_SB(1, 0), b3, voffB); PG8_STAGE(PG8_SB(1, 1), b3 + hstepB, voffB); PG8_STAGE(PG8_SA(1, 0), a3, voffA);
;             PG8_WAIT_V(8); PG8_WAIT_L(0); PG8_BAR; PG8_MMA(1, 0, At, B0); PG8_MMA(1, 1, At, B1); PG8_BAR; PG8_SCHED;
.Lkr5_b:
	s_waitcnt vmcnt(6)
	s_waitcnt lgkmcnt(0)
	s_barrier
	s_setprio 1
	s_waitcnt lgkmcnt(0)
	v_mfma_scale_f32_16x16x128_f8f6f4 v[94:97], v[2:9], v[212:219], v[94:97], v200, v201 op_sel_hi:[0,0,0]
	v_mfma_scale_f32_16x16x128_f8f6f4 v[90:93], v[10:17], v[212:219], v[90:93], v200, v201 op_sel_hi:[0,0,0]
	v_mfma_scale_f32_16x16x128_f8f6f4 v[78:81], v[2:9], v[220:227], v[78:81], v200, v201 op_sel_hi:[0,0,0]
	v_mfma_scale_f32_16x16x128_f8f6f4 v[74:77], v[10:17], v[220:227], v[74:77], v200, v201 op_sel_hi:[0,0,0]
	v_mfma_scale_f32_16x16x128_f8f6f4 v[62:65], v[2:9], v[228:235], v[62:65], v200, v201 op_sel_hi:[0,0,0]
	v_mfma_scale_f32_16x16x128_f8f6f4 v[58:61], v[10:17], v[228:235], v[58:61], v200, v201 op_sel_hi:[0,0,0]
	v_mfma_scale_f32_16x16x128_f8f6f4 v[46:49], v[2:9], v[236:243], v[46:49], v200, v201 op_sel_hi:[0,0,0]
	v_mfma_scale_f32_16x16x128_f8f6f4 v[42:45], v[10:17], v[236:243], v[42:45], v200, v201 op_sel_hi:[0,0,0]
	v_mfma_scale_f32_16x16x128_f8f6f4 v[86:89], v[18:25], v[212:219], v[86:89], v200, v201 op_sel_hi:[0,0,0]
	v_mfma_scale_f32_16x16x128_f8f6f4 v[82:85], v[26:33], v[212:219], v[82:85], v200, v201 op_sel_hi:[0,0,0]
	v_mfma_scale_f32_16x16x128_f8f6f4 v[70:73], v[18:25], v[220:227], v[70:73], v200, v201 op_sel_hi:[0,0,0]
	v_mfma_scale_f32_16x16x128_f8f6f4 v[66:69], v[26:33], v[220:227], v[66:69], v200, v201 op_sel_hi:[0,0,0]
	v_mfma_scale_f32_16x16x128_f8f6f4 v[54:57], v[18:25], v[228:235], v[54:57], v200, v201 op_sel_hi:[0,0,0]
	v_mfma_scale_f32_16x16x128_f8f6f4 v[50:53], v[26:33], v[228:235], v[50:53], v200, v201 op_sel_hi:[0,0,0]
	v_mfma_scale_f32_16x16x128_f8f6f4 v[38:41], v[18:25], v[236:243], v[38:41], v200, v201 op_sel_hi:[0,0,0]
	v_mfma_scale_f32_16x16x128_f8f6f4 v[34:37], v[26:33], v[236:243], v[34:37], v200, v201 op_sel_hi:[0,0,0]
	s_setprio 0
	s_add_u32 s46, s46, 0x100
	s_addc_u32 s47, s47, 0
	s_add_u32 s80, s80, 0x100
	s_addc_u32 s81, s81, 0
	s_cmp_ge_i32 s82, s58
	s_cselect_b32 s99, 0, 1
	s_mov_b32 s48, s82
	s_barrier
	s_cbranch_scc0 .LBB0_1625

; #define PG8_STAGE(bufoff, gbase, voff) do { _Pragma("unroll") for (int _i = 0; _i < 2; ++_i) \
;         __builtin_amdgcn_global_load_lds((const unsigned*)((const char*)(gbase) + (voff)[_i]), (PG8_LAS unsigned*)(lds + (bufoff) + ldsw + _i * 8192), 16, 0, 0); } while (0)
; #define PG8_LDA(dst, b, h) do { _Pragma("unroll") for (int m = 0; m < 4; ++m) { const bf16x8 f0_ = *(const PG8_LAS bf16x8*)(lds + PG8_SA(b, h) + aoff + m * 2048), f1_ = *(const PG8_LAS bf16x8*)(lds + PG8_SA(b, h) + aoff + m * 2048 + 1024); dst[m].set(f0_, f1_); } } while (0)
; #define PG8_WAIT_V(n) asm volatile("s_waitcnt vmcnt(" #n ")" ::: "memory")
; #define PG8_WAIT_L(n) asm volatile("s_waitcnt lgkmcnt(" #n ")" ::: "memory")
; #define PG8_BAR __builtin_amdgcn_s_barrier()
; #define PG8_SCHED __builtin_amdgcn_sched_barrier(0)
; template <class Epi, class Sched, bool ALIGN_EPI = false, bool SP2 = false>
; __device__ __forceinline__ void gemm_phase(PG8_LAS unsigned char* lds, const Gemm g, const Sched& S, const Epi& E) {
;     ...
;         for (int t = 0; t < nt; t += 2) {
;             if constexpr (Epi::MIDK) { if (t == (nt >> 1)) E.mid(acc, cur, wr, wc, fr, fq); }
;             const bool last = (t == nt - 2);
;             const char* a1 = cA + (size_t)(t + 1) * kstep;
;             const char* a2 = last ? nA : cA + (size_t)(t + 2) * kstep; const char* b2 = last ? nB : cB + (size_t)(t + 2) * kstep;
;     ...
;             PG8_LDA(At, 1, 1); PG8_STAGE(PG8_SB(1, 0), b3, voffB); PG8_STAGE(PG8_SB(1, 1), b3 + hstepB, voffB); PG8_STAGE(PG8_SA(1, 0), a3, voffA);
;             PG8_WAIT_V(8); PG8_WAIT_L(0); PG8_BAR; PG8_MMA(1, 0, At, B0); PG8_MMA(1, 1, At, B1); PG8_BAR; PG8_SCHED;
.Lkr6_b:
	s_waitcnt vmcnt(6)
	s_waitcnt lgkmcnt(0)
	s_barrier
	s_setprio 1
	s_waitcnt lgkmcnt(0)
	v_mfma_scale_f32_16x16x128_f8f6f4 v[92:95], v[0:7], v[172:179], v[92:95], v218, v219 op_sel_hi:[0,0,0]
	v_mfma_scale_f32_16x16x128_f8f6f4 v[88:91], v[8:15], v[172:179], v[88:91], v218, v219 op_sel_hi:[0,0,0]
	v_mfma_scale_f32_16x16x128_f8f6f4 v[76:79], v[0:7], v[226:233], v[76:79], v218, v219 op_sel_hi:[0,0,0]
	v_mfma_scale_f32_16x16x128_f8f6f4 v[72:75], v[8:15], v[226:233], v[72:75], v218, v219 op_sel_hi:[0,0,0]
	v_mfma_scale_f32_16x16x128_f8f6f4 v[60:63], v[0:7], v[234:241], v[60:63], v218, v219 op_sel_hi:[0,0,0]
	v_mfma_scale_f32_16x16x128_f8f6f4 v[56:59], v[8:15], v[234:241], v[56:59], v218, v219 op_sel_hi:[0,0,0]
	v_mfma_scale_f32_16x16x128_f8f6f4 v[44:47], v[0:7], v[242:249], v[44:47], v218, v219 op_sel_hi:[0,0,0]
	v_mfma_scale_f32_16x16x128_f8f6f4 v[40:43], v[8:15], v[242:249], v[40:43], v218, v219 op_sel_hi:[0,0,0]
	v_mfma_scale_f32_16x16x128_f8f6f4 v[84:87], v[16:23], v[172:179], v[84:87], v218, v219 op_sel_hi:[0,0,0]
	v_mfma_scale_f32_16x16x128_f8f6f4 v[80:83], v[24:31], v[172:179], v[80:83], v218, v219 op_sel_hi:[0,0,0]
	v_mfma_scale_f32_16x16x128_f8f6f4 v[68:71], v[16:23], v[226:233], v[68:71], v218, v219 op_sel_hi:[0,0,0]
	v_mfma_scale_f32_16x16x128_f8f6f4 v[64:67], v[24:31], v[226:233], v[64:67], v218, v219 op_sel_hi:[0,0,0]
	v_mfma_scale_f32_16x16x128_f8f6f4 v[52:55], v[16:23], v[234:241], v[52:55], v218, v219 op_sel_hi:[0,0,0]
	v_mfma_scale_f32_16x16x128_f8f6f4 v[48:51], v[24:31], v[234:241], v[48:51], v218, v219 op_sel_hi:[0,0,0]
	v_mfma_scale_f32_16x16x128_f8f6f4 v[36:39], v[16:23], v[242:249], v[36:39], v218, v219 op_sel_hi:[0,0,0]
	v_mfma_scale_f32_16x16x128_f8f6f4 v[32:35], v[24:31], v[242:249], v[32:35], v218, v219 op_sel_hi:[0,0,0]
	s_setprio 0
	s_add_u32 s2, s2, 0x100
	s_addc_u32 s3, s3, 0
	s_add_u32 s57, s57, 0x100
	s_addc_u32 s82, s82, 0
	s_cmp_ge_i32 s83, s91
	s_cselect_b32 s99, 0, 1
	s_mov_b32 s78, s83
	s_barrier
	s_cbranch_scc0 .LBB0_1658
